# out-projection: first two row groups of x fetched during the grid barrier in front of the phase instead of right before the K-loop (whose counted waits stalled on them)
# baseline (speedup 1.0000x reference)
;     __device__ __forceinline__ void operator()(AccRef acc, const Unit& u, int wr, int wc, int fr, int fq) const {
;     ...
;             for (int m = 0; m < 4; ++m) { const size_t ro = (size_t)(row0 + ai * HALF + m * 16) * DM + col0;
;                 f32x4 xv[2][2];
; #pragma unroll
;                 for (int bj = 0; bj < 2; ++bj)
; #pragma unroll
;                     for (int n = 0; n < 2; ++n) xv[bj][n] = __builtin_nontemporal_load((const f32x4*)(X + ro + bj * HALF + 4 * n));
; __device__ __forceinline__ void xcd_barrier(const XcdBarrier& b, const int tid) {
;     asm volatile("s_waitcnt vmcnt(0)" ::: "memory");
;     __syncthreads();
;     if (tid == 0) {
;         unsigned* bar = b.bar;
;         __builtin_amdgcn_s_waitcnt(0);
;         unsigned nloc = b.st[0], nx = b.st[1];
;         if (nloc == 0u) { xcd_barrier_complete(bar, b.x, nloc, nx); b.st[0] = nloc; b.st[1] = nx; }
.LBB0_414:
	s_cmp_gt_i32 s95, 3
	s_cbranch_scc0 .LBB0_468
	s_waitcnt vmcnt(19)
	v_mbcnt_lo_u32_b32 v0, -1, 0
	v_mbcnt_hi_u32_b32 v0, -1, v0
	s_waitcnt vmcnt(0)
	s_nop 0
	v_sub_u32_e32 v0, 0, v0
	v_cmp_eq_u32_e32 vcc, s93, v0
	s_barrier
	s_cmp_eq_u32 s92, 0
	s_cbranch_scc1 .Lxp2_w0
	s_and_b32 s98, s2, 7
	s_lshl_b32 s98, s98, 5
	s_lshr_b32 s99, s2, 3
	s_add_i32 s98, s98, s99
	s_lshr_b32 s99, s98, 6
	s_lshl_b32 s99, s99, 3
	s_and_b32 s100, s98, 7
	s_add_i32 s99, s99, s100
	s_lshl_b32 s99, s99, 8
	s_lshr_b32 s100, s92, 2
	s_lshl_b32 s100, s100, 6
	s_add_i32 s99, s99, s100
	s_bfe_u32 s100, s98, 0x30003
	s_lshl_b32 s100, s100, 8
	s_and_b32 s101, s92, 3
	s_lshl_b32 s101, s101, 5
	s_or_b32 s100, s100, s101
	v_mbcnt_lo_u32_b32 v240, -1, 0
	v_mbcnt_hi_u32_b32 v240, -1, v240
	v_and_or_b32 v241, v240, 15, s99
	v_ashrrev_i32_e32 v254, 1, v240
	v_and_b32_e32 v254, -8, v254
	v_add_u32_e32 v254, s100, v254
	v_lshl_add_u32 v254, v241, 11, v254
	v_lshlrev_b32_e32 v240, 2, v254
	global_load_dwordx4 v[208:211], v240, s[36:37] nt
	global_load_dwordx4 v[212:215], v240, s[36:37] offset:16 nt
	global_load_dwordx4 v[216:219], v240, s[36:37] offset:512 nt
	global_load_dwordx4 v[220:223], v240, s[36:37] offset:528 nt
	s_add_u32 s98, s36, 0x20000
	s_addc_u32 s99, s37, 0
	global_load_dwordx4 v[224:227], v240, s[98:99] nt
	global_load_dwordx4 v[228:231], v240, s[98:99] offset:16 nt
	global_load_dwordx4 v[232:235], v240, s[98:99] offset:512 nt
	global_load_dwordx4 v[236:239], v240, s[98:99] offset:528 nt
.Lxp2_w0:
	s_and_saveexec_b64 s[0:1], vcc
	s_cbranch_execz .LBB0_467
	s_add_i32 s4, 0, 0x22600
	v_mov_b32_e32 v0, s4
	s_waitcnt vmcnt(0) expcnt(0) lgkmcnt(0)
	ds_read_b32 v2, v0
	s_add_i32 s4, 0, 0x22604
	v_mov_b32_e32 v0, s4
	ds_read_b32 v0, v0
	s_waitcnt lgkmcnt(1)
	v_cmp_ne_u32_e32 vcc, 0, v2
	s_cbranch_vccnz .LBB0_431
	v_readlane_b32 s4, v255, 0
	v_readlane_b32 s5, v255, 1
	s_load_dwordx2 s[12:13], s[4:5], 0x4
	s_add_u32 s4, s26, 0x1000
	s_addc_u32 s5, s27, 0
	s_add_u32 s6, s26, 0x1100
	s_addc_u32 s7, s27, 0
	s_waitcnt lgkmcnt(0)
	s_mul_i32 s33, s12, s3
	s_add_u32 s12, s26, 0x1200
	s_mul_i32 s33, s33, s13
	s_addc_u32 s13, s27, 0
	s_add_u32 s16, s26, 0x1300
	s_addc_u32 s17, s27, 0
	s_mov_b32 s42, 1
	v_mov_b32_e32 v16, 0
	s_branch .LBB0_419

; __device__ __forceinline__ unsigned xb_ld(unsigned* p)              { return __hip_atomic_load(p, __ATOMIC_RELAXED, __HIP_MEMORY_SCOPE_AGENT); }
; __device__ __forceinline__ unsigned xb_add(unsigned* p, unsigned v) { return __hip_atomic_fetch_add(p, v, __ATOMIC_RELAXED, __HIP_MEMORY_SCOPE_AGENT); }
; #define XB_SPIN(cond, bar) do { unsigned _sp = 0; while (cond) { __builtin_amdgcn_s_sleep(1); \
;     if ((++_sp & 255u) == 0u) { if (xb_ld(&(bar)[XB_TMO])) break; if (_sp > XB_SPIN_CAP) { atomicAdd(&(bar)[XB_TMO], 1u); break; } } } } while (0)
;     __device__ __forceinline__ void operator()(AccRef acc, const Unit& u, int wr, int wc, int fr, int fq) const {
;     ...
;             for (int m = 0; m < 4; ++m) { const size_t ro = (size_t)(row0 + ai * HALF + m * 16) * DM + col0;
;                 f32x4 xv[2][2];
; #pragma unroll
;                 for (int bj = 0; bj < 2; ++bj)
; #pragma unroll
;                     for (int n = 0; n < 2; ++n) xv[bj][n] = __builtin_nontemporal_load((const f32x4*)(X + ro + bj * HALF + 4 * n));
; __device__ __forceinline__ void xcd_barrier(const XcdBarrier& b, const int tid) {
;     ...
;         const unsigned old = xb_add(&bar[XB_XSUB(b.x)], 1u);
;         const unsigned gen = old / nloc;
;         if (old + 1u == (gen + 1u) * nloc) {
;             __builtin_amdgcn_fence(__ATOMIC_RELEASE, "agent");
;             asm volatile("s_waitcnt vmcnt(0)" ::: "memory");
;             const unsigned og = xb_add(&bar[XB_TOP], 1u);
;             const unsigned tg = og / nx;
;             if (og + 1u == (tg + 1u) * nx) xb_add(&bar[XB_TOPGEN], 1u);
;             else XB_SPIN(xb_ld(&bar[XB_TOPGEN]) == tg, bar);
.LBB0_433:
	s_or_b64 exec, exec, s[12:13]
	buffer_inv sc1
	s_mov_b64 exec, -1
	s_and_b32 s98, s2, 7
	s_lshl_b32 s98, s98, 5
	s_lshr_b32 s99, s2, 3
	s_add_i32 s98, s98, s99
	s_lshr_b32 s99, s98, 6
	s_lshl_b32 s99, s99, 3
	s_and_b32 s100, s98, 7
	s_add_i32 s99, s99, s100
	s_lshl_b32 s99, s99, 8
	s_lshr_b32 s100, s92, 2
	s_lshl_b32 s100, s100, 6
	s_add_i32 s99, s99, s100
	s_bfe_u32 s100, s98, 0x30003
	s_lshl_b32 s100, s100, 8
	s_and_b32 s101, s92, 3
	s_lshl_b32 s101, s101, 5
	s_or_b32 s100, s100, s101
	v_mbcnt_lo_u32_b32 v240, -1, 0
	v_mbcnt_hi_u32_b32 v240, -1, v240
	v_and_or_b32 v241, v240, 15, s99
	v_ashrrev_i32_e32 v254, 1, v240
	v_and_b32_e32 v254, -8, v254
	v_add_u32_e32 v254, s100, v254
	v_lshl_add_u32 v254, v241, 11, v254
	v_lshlrev_b32_e32 v240, 2, v254
	global_load_dwordx4 v[208:211], v240, s[36:37] nt
	global_load_dwordx4 v[212:215], v240, s[36:37] offset:16 nt
	global_load_dwordx4 v[216:219], v240, s[36:37] offset:512 nt
	global_load_dwordx4 v[220:223], v240, s[36:37] offset:528 nt
	s_add_u32 s98, s36, 0x20000
	s_addc_u32 s99, s37, 0
	global_load_dwordx4 v[224:227], v240, s[98:99] nt
	global_load_dwordx4 v[228:231], v240, s[98:99] offset:16 nt
	global_load_dwordx4 v[232:235], v240, s[98:99] offset:512 nt
	global_load_dwordx4 v[236:239], v240, s[98:99] offset:528 nt
	s_mov_b64 exec, 1
	v_cvt_f32_u32_e32 v4, v2
	s_waitcnt vmcnt(9)
	v_readfirstlane_b32 s6, v3
	v_sub_u32_e32 v3, 0, v2
	v_rcp_iflag_f32_e32 v4, v4
	v_add_u32_e32 v5, s6, v1
	v_mul_f32_e32 v4, 0x4f7ffffe, v4
	v_cvt_u32_f32_e32 v4, v4
	v_mul_lo_u32 v1, v3, v4
	v_mul_hi_u32 v1, v4, v1
	v_add_u32_e32 v1, v4, v1
	v_mul_hi_u32 v1, v5, v1
	v_mul_lo_u32 v3, v1, v2
	v_sub_u32_e32 v3, v5, v3
	v_add_u32_e32 v4, 1, v1
	v_cmp_ge_u32_e32 vcc, v3, v2
	s_nop 1
	v_cndmask_b32_e32 v1, v1, v4, vcc
	v_sub_u32_e32 v4, v3, v2
	v_cndmask_b32_e32 v3, v3, v4, vcc
	v_add_u32_e32 v4, 1, v1
	v_cmp_ge_u32_e32 vcc, v3, v2
	v_add_u32_e32 v3, 1, v5
	s_nop 0
	v_cndmask_b32_e32 v1, v1, v4, vcc
	v_mul_lo_u32 v4, v2, v1
	v_add_u32_e32 v2, v4, v2
	s_waitcnt lgkmcnt(0)
	v_add_u32_e32 v4, 1, v1
	v_mul_lo_u32 v4, v4, v0
	v_mov_b32_e32 v5, 0x3600
	v_cmp_ne_u32_e32 vcc, v3, v2
	s_cbranch_vccnz .Lgb2_wait
	buffer_wbl2 sc1
	s_waitcnt vmcnt(0) lgkmcnt(0)
	v_mov_b32_e32 v2, 1
	global_atomic_add v5, v2, s[26:27]
	global_atomic_add v5, v2, s[26:27] offset:256
	global_atomic_add v5, v2, s[26:27] offset:512
	global_atomic_add v5, v2, s[26:27] offset:768
	global_atomic_add v5, v2, s[26:27] offset:1024
	global_atomic_add v5, v2, s[26:27] offset:1280
	global_atomic_add v5, v2, s[26:27] offset:1536
	global_atomic_add v5, v2, s[26:27] offset:1792
